# final6 + grid barrier release path: at the 9 in-loop barrier sites the non-last XCD leaders poll the TOP arrival counter (>= (gen+1)*nx) instead of the TOPGEN word, one cross-XCD round trip less befor
# speedup vs baseline: 1.0189x; 1.0052x over previous
; __device__ __forceinline__ unsigned xb_ld(unsigned* p)              { return __hip_atomic_load(p, __ATOMIC_RELAXED, __HIP_MEMORY_SCOPE_AGENT); }
; __device__ __forceinline__ unsigned xb_add(unsigned* p, unsigned v) { return __hip_atomic_fetch_add(p, v, __ATOMIC_RELAXED, __HIP_MEMORY_SCOPE_AGENT); }
; #define XB_SPIN(cond, bar) do { unsigned _sp = 0; while (cond) { __builtin_amdgcn_s_sleep(1); \
;     if ((++_sp & 255u) == 0u) { if (xb_ld(&(bar)[XB_TMO])) break; if (_sp > XB_SPIN_CAP) { atomicAdd(&(bar)[XB_TMO], 1u); break; } } } } while (0)
; __device__ __forceinline__ void xcd_barrier(const XcdBarrier& b, const int tid) {
;     ...
;         const unsigned old = xb_add(&bar[XB_XSUB(b.x)], 1u);
;         const unsigned gen = old / nloc;
;         if (old + 1u == (gen + 1u) * nloc) {
;             __builtin_amdgcn_fence(__ATOMIC_RELEASE, "agent");
;             asm volatile("s_waitcnt vmcnt(0)" ::: "memory");
;             const unsigned og = xb_add(&bar[XB_TOP], 1u);
;             const unsigned tg = og / nx;
;             if (og + 1u == (tg + 1u) * nx) xb_add(&bar[XB_TOPGEN], 1u);
;             else XB_SPIN(xb_ld(&bar[XB_TOPGEN]) == tg, bar);
;             __builtin_amdgcn_fence(__ATOMIC_ACQUIRE, "agent");
.LBB0_747:
	s_or_b64 exec, exec, s[42:43]
	s_waitcnt vmcnt(0)
	v_readfirstlane_b32 s7, v3
	v_sub_u32_e32 v4, 0, v2
	v_readlane_b32 s22, v252, 15
	v_add_u32_e32 v3, s7, v0
	v_cvt_f32_u32_e32 v0, v2
	v_readlane_b32 s23, v252, 16
	s_mov_b64 s[42:43], -1
	v_rcp_iflag_f32_e32 v0, v0
	s_nop 0
	v_mul_f32_e32 v0, 0x4f7ffffe, v0
	v_cvt_u32_f32_e32 v0, v0
	v_mul_lo_u32 v4, v4, v0
	v_mul_hi_u32 v4, v0, v4
	v_add_u32_e32 v0, v0, v4
	v_mul_hi_u32 v0, v3, v0
	v_mul_lo_u32 v4, v0, v2
	v_sub_u32_e32 v4, v3, v4
	v_cmp_ge_u32_e32 vcc, v4, v2
	v_add_u32_e32 v5, 1, v0
	v_add_u32_e32 v3, 1, v3
	v_cndmask_b32_e32 v0, v0, v5, vcc
	v_sub_u32_e32 v5, v4, v2
	v_cndmask_b32_e32 v4, v4, v5, vcc
	v_cmp_ge_u32_e32 vcc, v4, v2
	v_add_u32_e32 v4, 1, v0
	s_nop 0
	v_cndmask_b32_e32 v0, v0, v4, vcc
	v_mul_lo_u32 v4, v2, v0
	v_add_u32_e32 v2, v4, v2
	v_cmp_ne_u32_e32 vcc, v3, v2
	v_mov_b32_e32 v5, v2
	v_mov_b64_e32 v[2:3], s[22:23]
	s_and_saveexec_b64 s[40:41], vcc
	s_cbranch_execz .LBB0_759
	v_readlane_b32 s22, v252, 13
	v_readlane_b32 s23, v252, 14
	s_mov_b64 s[44:45], 0
	s_nop 3
	global_load_dword v2, v1, s[22:23] sc1
	s_waitcnt vmcnt(0)
	v_cmp_lt_u32_e32 vcc, v2, v5
	s_and_saveexec_b64 s[42:43], vcc
	s_cbranch_execz .LBB0_758
	s_mov_b32 s7, 1
	s_branch .LBB0_751

; __device__ __forceinline__ unsigned xb_ld(unsigned* p)              { return __hip_atomic_load(p, __ATOMIC_RELAXED, __HIP_MEMORY_SCOPE_AGENT); }
; __device__ __forceinline__ unsigned xb_add(unsigned* p, unsigned v) { return __hip_atomic_fetch_add(p, v, __ATOMIC_RELAXED, __HIP_MEMORY_SCOPE_AGENT); }
; #define XB_SPIN(cond, bar) do { unsigned _sp = 0; while (cond) { __builtin_amdgcn_s_sleep(1); \
;     if ((++_sp & 255u) == 0u) { if (xb_ld(&(bar)[XB_TMO])) break; if (_sp > XB_SPIN_CAP) { atomicAdd(&(bar)[XB_TMO], 1u); break; } } } } while (0)
; __device__ __forceinline__ void xcd_barrier(const XcdBarrier& b, const int tid) {
;     ...
;             const unsigned og = xb_add(&bar[XB_TOP], 1u);
;             const unsigned tg = og / nx;
;             if (og + 1u == (tg + 1u) * nx) xb_add(&bar[XB_TOPGEN], 1u);
;             else XB_SPIN(xb_ld(&bar[XB_TOPGEN]) == tg, bar);
.LBB0_755:
	v_readlane_b32 s22, v252, 13
	v_readlane_b32 s23, v252, 14
	s_add_i32 s7, s7, 1
	s_mov_b64 s[54:55], -1
	s_nop 2
	global_load_dword v2, v1, s[22:23] sc1
	s_waitcnt vmcnt(0)
	v_cmp_ge_u32_e32 vcc, v2, v5
	s_orn2_b64 s[48:49], vcc, exec
	s_branch .LBB0_750

; __device__ __forceinline__ unsigned xb_ld(unsigned* p)              { return __hip_atomic_load(p, __ATOMIC_RELAXED, __HIP_MEMORY_SCOPE_AGENT); }
; __device__ __forceinline__ unsigned xb_add(unsigned* p, unsigned v) { return __hip_atomic_fetch_add(p, v, __ATOMIC_RELAXED, __HIP_MEMORY_SCOPE_AGENT); }
; #define XB_SPIN(cond, bar) do { unsigned _sp = 0; while (cond) { __builtin_amdgcn_s_sleep(1); \
;     if ((++_sp & 255u) == 0u) { if (xb_ld(&(bar)[XB_TMO])) break; if (_sp > XB_SPIN_CAP) { atomicAdd(&(bar)[XB_TMO], 1u); break; } } } } while (0)
; __device__ __forceinline__ void xcd_barrier(const XcdBarrier& b, const int tid) {
;     ...
;         const unsigned old = xb_add(&bar[XB_XSUB(b.x)], 1u);
;         const unsigned gen = old / nloc;
;         if (old + 1u == (gen + 1u) * nloc) {
;             __builtin_amdgcn_fence(__ATOMIC_RELEASE, "agent");
;             asm volatile("s_waitcnt vmcnt(0)" ::: "memory");
;             const unsigned og = xb_add(&bar[XB_TOP], 1u);
;             const unsigned tg = og / nx;
;             if (og + 1u == (tg + 1u) * nx) xb_add(&bar[XB_TOPGEN], 1u);
;             else XB_SPIN(xb_ld(&bar[XB_TOPGEN]) == tg, bar);
;             __builtin_amdgcn_fence(__ATOMIC_ACQUIRE, "agent");
.LBB0_1819:
	s_or_b64 exec, exec, s[42:43]
	s_waitcnt vmcnt(0)
	v_readfirstlane_b32 s6, v3
	v_sub_u32_e32 v4, 0, v2
	s_mov_b64 s[42:43], -1
	v_add_u32_e32 v3, s6, v0
	v_cvt_f32_u32_e32 v0, v2
	v_readlane_b32 s6, v252, 15
	v_readlane_b32 s7, v252, 16
	v_rcp_iflag_f32_e32 v0, v0
	s_nop 0
	v_mul_f32_e32 v0, 0x4f7ffffe, v0
	v_cvt_u32_f32_e32 v0, v0
	v_mul_lo_u32 v4, v4, v0
	v_mul_hi_u32 v4, v0, v4
	v_add_u32_e32 v0, v0, v4
	v_mul_hi_u32 v0, v3, v0
	v_mul_lo_u32 v4, v0, v2
	v_sub_u32_e32 v4, v3, v4
	v_cmp_ge_u32_e32 vcc, v4, v2
	v_add_u32_e32 v5, 1, v0
	v_add_u32_e32 v3, 1, v3
	v_cndmask_b32_e32 v0, v0, v5, vcc
	v_sub_u32_e32 v5, v4, v2
	v_cndmask_b32_e32 v4, v4, v5, vcc
	v_cmp_ge_u32_e32 vcc, v4, v2
	v_add_u32_e32 v4, 1, v0
	s_nop 0
	v_cndmask_b32_e32 v0, v0, v4, vcc
	v_mul_lo_u32 v4, v2, v0
	v_add_u32_e32 v2, v4, v2
	v_cmp_ne_u32_e32 vcc, v3, v2
	v_mov_b32_e32 v5, v2
	v_mov_b64_e32 v[2:3], s[6:7]
	s_and_saveexec_b64 s[40:41], vcc
	s_cbranch_execz .LBB0_1831
	v_readlane_b32 s6, v252, 13
	v_readlane_b32 s7, v252, 14
	s_mov_b64 s[44:45], 0
	s_nop 3
	global_load_dword v2, v1, s[6:7] sc1
	s_waitcnt vmcnt(0)
	v_cmp_lt_u32_e32 vcc, v2, v5
	s_and_saveexec_b64 s[42:43], vcc
	s_cbranch_execz .LBB0_1830
	s_mov_b32 s6, 1
	s_branch .LBB0_1823

; __device__ __forceinline__ unsigned xb_ld(unsigned* p)              { return __hip_atomic_load(p, __ATOMIC_RELAXED, __HIP_MEMORY_SCOPE_AGENT); }
; __device__ __forceinline__ unsigned xb_add(unsigned* p, unsigned v) { return __hip_atomic_fetch_add(p, v, __ATOMIC_RELAXED, __HIP_MEMORY_SCOPE_AGENT); }
; #define XB_SPIN(cond, bar) do { unsigned _sp = 0; while (cond) { __builtin_amdgcn_s_sleep(1); \
;     if ((++_sp & 255u) == 0u) { if (xb_ld(&(bar)[XB_TMO])) break; if (_sp > XB_SPIN_CAP) { atomicAdd(&(bar)[XB_TMO], 1u); break; } } } } while (0)
; __device__ __forceinline__ void xcd_barrier(const XcdBarrier& b, const int tid) {
;     ...
;             const unsigned og = xb_add(&bar[XB_TOP], 1u);
;             const unsigned tg = og / nx;
;             if (og + 1u == (tg + 1u) * nx) xb_add(&bar[XB_TOPGEN], 1u);
;             else XB_SPIN(xb_ld(&bar[XB_TOPGEN]) == tg, bar);
.LBB0_1827:
	v_readlane_b32 s22, v252, 13
	v_readlane_b32 s23, v252, 14
	s_add_i32 s6, s6, 1
	s_mov_b64 s[54:55], -1
	s_nop 2
	global_load_dword v2, v1, s[22:23] sc1
	s_waitcnt vmcnt(0)
	v_cmp_ge_u32_e32 vcc, v2, v5
	s_orn2_b64 s[48:49], vcc, exec
	s_branch .LBB0_1822
